# x14v5: scan y stores packed to dword write-through stores (2 per chunk instead of 4 shorts)
# speedup vs baseline: 1.0415x; 1.0055x over previous
.LBB0_1725:
	s_cmp_eq_u32 s82, 0
	s_cbranch_scc1 .Lx14_w0
	s_waitcnt vmcnt(8)
	s_branch .Lx14_wj
.Lx14_w0:
	s_waitcnt vmcnt(9)

.LBB0_1734:
	s_mul_i32 s0, s69, 0x3300
	s_add_i32 s0, s74, s0
	s_add_i32 s1, s0, 0x2a00
	v_add_u32_e32 v18, s1, v185
	ds_read_b64_tr_b16 v[20:21], v18
	v_add3_u32 v18, s0, v186, v187
	ds_read2_b64 v[26:29], v18 offset1:4
	ds_read2_b64 v[30:33], v18 offset0:8 offset1:12
	v_add_u32_e32 v18, 0x800, v18
	v_cvt_pk_bf16_f32 v22, v2, v3
	v_cvt_pk_bf16_f32 v23, v4, v5
	v_cvt_pk_bf16_f32 v24, v10, v11
	v_cvt_pk_bf16_f32 v25, v12, v13
	ds_read2_b64 v[38:41], v18 offset0:32 offset1:36
	ds_read2_b64 v[42:45], v18 offset0:40 offset1:44
	s_waitcnt lgkmcnt(3)
	v_mfma_f32_16x16x32_bf16 v[26:29], v[26:29], v[22:25], 0
	s_waitcnt lgkmcnt(0)
	s_add_i32 s76, s69, s68
	v_cvt_pk_bf16_f32 v34, v6, v7
	v_cvt_pk_bf16_f32 v35, v8, v9
	v_cvt_pk_bf16_f32 v36, v14, v15
	v_cvt_pk_bf16_f32 v37, v16, v17
	s_waitcnt lgkmcnt(2)
	s_nop 0
	v_mfma_f32_16x16x32_bf16 v[26:29], v[30:33], v[34:37], v[26:29]
	s_nop 7
	v_cvt_pk_bf16_f32 v18, v26, v27
	v_add_u32_e32 v26, s0, v192
	ds_read_b128 v[30:33], v26 offset:8704
	v_add_u32_e32 v62, s0, v191
	ds_read_b128 v[46:49], v62 offset:12800
	v_cvt_pk_bf16_f32 v19, v28, v29
	ds_read_b128 v[26:29], v26 offset:9728
	ds_read_b128 v[50:53], v62 offset:12864
	v_add_u32_e32 v63, v62, v190
	ds_read_b128 v[54:57], v63 offset:4608
	ds_read_b128 v[58:61], v63 offset:5632
	s_waitcnt lgkmcnt(5)
	v_mfma_f32_16x16x32_bf16 v[30:33], v[30:33], v[18:21], 0
	s_waitcnt lgkmcnt(2)
	v_pk_mul_f32 v[10:11], v[10:11], v[50:51]
	v_pk_mul_f32 v[12:13], v[12:13], v[52:53]
	ds_read_b128 v[50:53], v63 offset:7680
	v_mfma_f32_16x16x32_bf16 v[22:25], v[38:41], v[22:25], 0
	s_nop 2
	v_cvt_pk_bf16_f32 v18, v30, v31
	v_cvt_pk_bf16_f32 v19, v32, v33
	ds_read_b128 v[30:33], v63 offset:6656
	v_pk_mul_f32 v[2:3], v[2:3], v[46:47]
	v_pk_mul_f32 v[4:5], v[4:5], v[48:49]
	ds_read_b128 v[46:49], v62 offset:12928
	v_mfma_f32_16x16x32_bf16 v[22:25], v[42:45], v[34:37], v[22:25]
	s_cmp_lt_u32 s76, 16
	s_waitcnt lgkmcnt(4)
	v_mfma_f32_16x16x32_bf16 v[2:5], v[54:57], v[18:21], v[2:5]
	ds_read_b128 v[54:57], v62 offset:12992
	s_waitcnt lgkmcnt(1)
	v_pk_mul_f32 v[6:7], v[6:7], v[46:47]
	v_pk_mul_f32 v[8:9], v[8:9], v[48:49]
	v_mfma_f32_16x16x32_bf16 v[10:13], v[58:61], v[18:21], v[10:13]
	s_waitcnt lgkmcnt(0)
	v_pk_mul_f32 v[14:15], v[14:15], v[54:55]
	v_pk_mul_f32 v[16:17], v[16:17], v[56:57]
	v_mfma_f32_16x16x32_bf16 v[6:9], v[30:33], v[18:21], v[6:9]
	s_nop 0
	v_mfma_f32_16x16x32_bf16 v[14:17], v[50:53], v[18:21], v[14:17]
	v_mfma_f32_16x16x32_bf16 v[18:21], v[26:29], v[18:21], v[22:25]
	s_cbranch_scc1 .LBB0_1731
	s_nop 1
	v_and_b32_e32 v25, 1, v0
	v_lshl_or_b32 v24, s76, 4, v184
	v_add_u32_e32 v24, v24, v25
	v_add_u32_e32 v22, 0xffffff00, v24
	v_sub_u32_e32 v23, 0x40ff, v24
	v_cndmask_b32_e64 v22, v23, v22, s[28:29]
	v_add_u32_e32 v22, s70, v22
	v_ashrrev_i32_e32 v23, 31, v22
	v_lshlrev_b64 v[22:23], 12, v[22:23]
	v_lshl_add_u64 v[22:23], v[164:165], 0, v[22:23]
	v_sub_u32_e32 v27, 0, v25
	v_lshlrev_b32_e32 v26, 1, v27
	v_lshl_add_u64 v[22:23], v[22:23], 0, v[26:27]
	v_mov_b32_e32 v28, 0x2000
	v_mov_b32_e32 v29, 0xffffe000
	v_cndmask_b32_e64 v28, v29, v28, s[28:29]
	v_ashrrev_i32_e32 v29, 31, v28
	v_lshl_add_u64 v[30:31], v[22:23], 0, v[28:29]
	v_cmp_ne_u32_e32 vcc, 0, v25
	v_mov_b32_dpp v32, v18 quad_perm:[1,0,3,2] row_mask:0xf bank_mask:0xf bound_ctrl:1
	v_mov_b32_dpp v33, v19 quad_perm:[1,0,3,2] row_mask:0xf bank_mask:0xf bound_ctrl:1
	v_mov_b32_dpp v34, v20 quad_perm:[1,0,3,2] row_mask:0xf bank_mask:0xf bound_ctrl:1
	v_mov_b32_dpp v35, v21 quad_perm:[1,0,3,2] row_mask:0xf bank_mask:0xf bound_ctrl:1
	v_cndmask_b32_e32 v36, v18, v33, vcc
	v_cndmask_b32_e32 v37, v32, v19, vcc
	v_cndmask_b32_e32 v38, v20, v35, vcc
	v_cndmask_b32_e32 v39, v34, v21, vcc
	v_cvt_pk_bf16_f32 v36, v36, v37
	v_cvt_pk_bf16_f32 v38, v38, v39
	global_store_dword v[22:23], v36, off sc1
	global_store_dword v[30:31], v38, off sc1
	s_branch .LBB0_1731
